# P8 Wo epilogue: prefetch residual x lines into L2 with early dword loads (breaks 16-step HBM round-trip chain)
# speedup vs baseline: 1.0404x; 1.0404x over previous
;     __device__ __forceinline__ void operator()(const f32x4 (&acc)[2][2][4][2], const Unit& u, int wr, int wc, int fr, int fq) const {
;         const int row0 = u.pm * BM + wr * 64 + fr, col0 = u.pn * BM + wc * 32 + 8 * fq;
;         f32x4 gv[2][2];
; #pragma unroll
;         for (int bj = 0; bj < 2; ++bj)
; #pragma unroll
;             for (int n = 0; n < 2; ++n) gv[bj][n] = *(const f32x4*)(gate + col0 + bj * HALF + n * 4);
; #pragma unroll
;         for (int ai = 0; ai < 2; ++ai)
; #pragma unroll
;             for (int m = 0; m < 4; ++m) { const size_t off = (size_t)(row0 + ai * HALF + m * 16) * DM + col0;
; #pragma unroll
;                 for (int bj = 0; bj < 2; ++bj) { const f32x4 x0 = *(const f32x4*)(x + off + bj * HALF), x1 = *(const f32x4*)(x + off + bj * HALF + 4);
;                     *(u32x4*)(out + off + bj * HALF) = pack8s(x0 + gv[bj][0] * acc[ai][bj][m][0], x1 + gv[bj][1] * acc[ai][bj][m][1], 1.f); }
;                 if (m & 1) asm volatile("" ::: "memory"); }
.LBB0_1331:
	v_lshl_add_u32 v160, s74, 8, v165
	v_lshl_or_b32 v158, s75, 8, v167
	v_ashrrev_i32_e32 v161, 31, v160
	v_ashrrev_i32_e32 v159, 31, v158
	v_lshlrev_b64 v[130:131], 11, v[160:161]
	v_lshl_add_u64 v[156:157], v[130:131], 0, v[158:159]
	v_lshl_add_u64 v[134:135], v[158:159], 2, s[24:25]
	s_waitcnt lgkmcnt(0)
	v_lshl_add_u64 v[184:185], v[156:157], 2, s[10:11]
	global_load_dwordx4 v[176:179], v[184:185], off
	global_load_dwordx4 v[142:145], v[134:135], off
	global_load_dwordx4 v[138:141], v[134:135], off offset:16
	global_load_dwordx4 v[180:183], v[184:185], off offset:16
	global_load_dwordx4 v[130:133], v[134:135], off offset:528
	s_nop 0
	global_load_dwordx4 v[134:137], v[134:135], off offset:512
	v_mov_b32_e32 v188, 0x20000
	v_mov_b32_e32 v189, 0
	global_load_dword v192, v[184:185], off offset:512
	v_lshl_add_u64 v[190:191], v[184:185], 0, v[188:189]
	global_load_dword v193, v[190:191], off
	global_load_dword v194, v[190:191], off offset:512
	v_lshl_add_u64 v[190:191], v[190:191], 0, v[188:189]
	global_load_dword v195, v[190:191], off
	global_load_dword v196, v[190:191], off offset:512
	v_lshl_add_u64 v[190:191], v[190:191], 0, v[188:189]
	global_load_dword v197, v[190:191], off
	global_load_dword v198, v[190:191], off offset:512
	v_mov_b32_e32 v188, 0x100000
	s_nop 0
	v_lshl_add_u64 v[190:191], v[184:185], 0, v[188:189]
	v_mov_b32_e32 v188, 0x20000
	global_load_dword v199, v[190:191], off
	global_load_dword v200, v[190:191], off offset:512
	v_lshl_add_u64 v[190:191], v[190:191], 0, v[188:189]
	global_load_dword v201, v[190:191], off
	global_load_dword v202, v[190:191], off offset:512
	v_lshl_add_u64 v[190:191], v[190:191], 0, v[188:189]
	global_load_dword v203, v[190:191], off
	global_load_dword v204, v[190:191], off offset:512
	v_lshl_add_u64 v[190:191], v[190:191], 0, v[188:189]
	global_load_dword v205, v[190:191], off
	global_load_dword v206, v[190:191], off offset:512
	v_lshl_add_u64 v[186:187], v[156:157], 1, s[38:39]
	s_and_b64 vcc, exec, s[4:5]
	s_mov_b64 s[4:5], -1
	s_waitcnt vmcnt(0)
	v_pk_fma_f32 v[126:127], v[126:127], v[142:143], v[176:177]
	v_pk_fma_f32 v[128:129], v[128:129], v[144:145], v[178:179]
	v_pk_fma_f32 v[176:177], v[124:125], v[140:141], v[182:183]
	v_pk_fma_f32 v[124:125], v[122:123], v[138:139], v[180:181]
	v_cvt_pk_bf16_f32 v122, v126, v127
	v_cvt_pk_bf16_f32 v123, v128, v129
	s_nop 0
	v_cvt_pk_bf16_f32 v124, v124, v125
	v_cvt_pk_bf16_f32 v125, v176, v177
	global_store_dwordx4 v[186:187], v[122:125], off
	global_load_dwordx4 v[122:125], v[184:185], off offset:512
	s_nop 0
	global_load_dwordx4 v[126:129], v[184:185], off offset:528
	v_or_b32_e32 v176, 16, v160
	v_ashrrev_i32_e32 v177, 31, v176
	v_lshlrev_b64 v[176:177], 11, v[176:177]
	v_lshl_add_u64 v[176:177], v[176:177], 0, v[158:159]
	v_lshl_add_u64 v[178:179], v[176:177], 2, s[10:11]
	s_waitcnt vmcnt(1)
	v_pk_fma_f32 v[118:119], v[118:119], v[134:135], v[122:123]
	s_waitcnt vmcnt(0)
	v_pk_fma_f32 v[122:123], v[116:117], v[132:133], v[128:129]
	v_pk_fma_f32 v[116:117], v[114:115], v[130:131], v[126:127]
	v_pk_fma_f32 v[120:121], v[120:121], v[136:137], v[124:125]
	v_cvt_pk_bf16_f32 v114, v118, v119
	s_nop 0
	v_cvt_pk_bf16_f32 v115, v120, v121
	v_cvt_pk_bf16_f32 v116, v116, v117
	v_cvt_pk_bf16_f32 v117, v122, v123
	global_store_dwordx4 v[186:187], v[114:117], off offset:256
	global_load_dwordx4 v[114:117], v[178:179], off
	s_nop 0
	global_load_dwordx4 v[118:121], v[178:179], off offset:16
	v_lshl_add_u64 v[122:123], v[176:177], 1, s[38:39]
	s_waitcnt vmcnt(1)
	v_pk_fma_f32 v[110:111], v[110:111], v[142:143], v[114:115]
	s_waitcnt vmcnt(0)
	v_pk_fma_f32 v[114:115], v[108:109], v[140:141], v[120:121]
	v_pk_fma_f32 v[108:109], v[106:107], v[138:139], v[118:119]
	v_pk_fma_f32 v[112:113], v[112:113], v[144:145], v[116:117]
	v_cvt_pk_bf16_f32 v106, v110, v111
	s_nop 0
	v_cvt_pk_bf16_f32 v107, v112, v113
	v_cvt_pk_bf16_f32 v108, v108, v109
	v_cvt_pk_bf16_f32 v109, v114, v115
	global_store_dwordx4 v[122:123], v[106:109], off
	global_load_dwordx4 v[106:109], v[178:179], off offset:512
	s_nop 0
	global_load_dwordx4 v[110:113], v[178:179], off offset:528
	v_or_b32_e32 v114, 32, v160
	v_ashrrev_i32_e32 v115, 31, v114
	v_lshlrev_b64 v[114:115], 11, v[114:115]
	v_lshl_add_u64 v[114:115], v[114:115], 0, v[158:159]
	v_lshl_add_u64 v[116:117], v[114:115], 2, s[10:11]
	s_waitcnt vmcnt(1)
	v_pk_fma_f32 v[102:103], v[102:103], v[134:135], v[106:107]
	s_waitcnt vmcnt(0)
	v_pk_fma_f32 v[106:107], v[100:101], v[132:133], v[112:113]
	v_pk_fma_f32 v[100:101], v[98:99], v[130:131], v[110:111]
	v_pk_fma_f32 v[104:105], v[104:105], v[136:137], v[108:109]
	v_cvt_pk_bf16_f32 v98, v102, v103
	s_nop 0
	v_cvt_pk_bf16_f32 v99, v104, v105
	v_cvt_pk_bf16_f32 v100, v100, v101
	v_cvt_pk_bf16_f32 v101, v106, v107
	global_store_dwordx4 v[122:123], v[98:101], off offset:256
	global_load_dwordx4 v[98:101], v[116:117], off
	global_load_dwordx4 v[102:105], v[116:117], off offset:16
	v_lshl_add_u64 v[106:107], v[114:115], 1, s[38:39]
	s_waitcnt vmcnt(1)
	v_pk_fma_f32 v[94:95], v[94:95], v[142:143], v[98:99]
	s_waitcnt vmcnt(0)
	v_pk_fma_f32 v[98:99], v[92:93], v[140:141], v[104:105]
	v_pk_fma_f32 v[92:93], v[90:91], v[138:139], v[102:103]
	v_pk_fma_f32 v[96:97], v[96:97], v[144:145], v[100:101]
	v_cvt_pk_bf16_f32 v90, v94, v95
	s_nop 0
	v_cvt_pk_bf16_f32 v91, v96, v97
	v_cvt_pk_bf16_f32 v92, v92, v93
	v_cvt_pk_bf16_f32 v93, v98, v99
	global_store_dwordx4 v[106:107], v[90:93], off
	global_load_dwordx4 v[90:93], v[116:117], off offset:512
	s_nop 0
	global_load_dwordx4 v[94:97], v[116:117], off offset:528
	v_or_b32_e32 v98, 48, v160
	v_ashrrev_i32_e32 v99, 31, v98
	v_lshlrev_b64 v[98:99], 11, v[98:99]
	v_lshl_add_u64 v[98:99], v[98:99], 0, v[158:159]
	v_lshl_add_u64 v[100:101], v[98:99], 2, s[10:11]
	s_waitcnt vmcnt(1)
;     __device__ __forceinline__ void operator()(const f32x4 (&acc)[2][2][4][2], const Unit& u, int wr, int wc, int fr, int fq) const {
;     ...
;         for (int ai = 0; ai < 2; ++ai)
; #pragma unroll
;             for (int m = 0; m < 4; ++m) { const size_t off = (size_t)(row0 + ai * HALF + m * 16) * DM + col0;
; #pragma unroll
;                 for (int bj = 0; bj < 2; ++bj) { const f32x4 x0 = *(const f32x4*)(x + off + bj * HALF), x1 = *(const f32x4*)(x + off + bj * HALF + 4);
;                     *(u32x4*)(out + off + bj * HALF) = pack8s(x0 + gv[bj][0] * acc[ai][bj][m][0], x1 + gv[bj][1] * acc[ai][bj][m][1], 1.f); }
;                 if (m & 1) asm volatile("" ::: "memory"); }
	v_pk_fma_f32 v[86:87], v[86:87], v[134:135], v[90:91]
	s_waitcnt vmcnt(0)
	v_pk_fma_f32 v[90:91], v[84:85], v[132:133], v[96:97]
	v_pk_fma_f32 v[84:85], v[82:83], v[130:131], v[94:95]
	v_pk_fma_f32 v[88:89], v[88:89], v[136:137], v[92:93]
	v_cvt_pk_bf16_f32 v82, v86, v87
	s_nop 0
	v_cvt_pk_bf16_f32 v83, v88, v89
	v_cvt_pk_bf16_f32 v84, v84, v85
	v_cvt_pk_bf16_f32 v85, v90, v91
	global_store_dwordx4 v[106:107], v[82:85], off offset:256
	global_load_dwordx4 v[82:85], v[100:101], off
	s_nop 0
	global_load_dwordx4 v[86:89], v[100:101], off offset:16
	v_lshl_add_u64 v[90:91], v[98:99], 1, s[38:39]
	s_waitcnt vmcnt(1)
	v_pk_fma_f32 v[78:79], v[78:79], v[142:143], v[82:83]
	s_waitcnt vmcnt(0)
	v_pk_fma_f32 v[82:83], v[76:77], v[140:141], v[88:89]
	v_pk_fma_f32 v[76:77], v[74:75], v[138:139], v[86:87]
	v_pk_fma_f32 v[80:81], v[80:81], v[144:145], v[84:85]
	v_cvt_pk_bf16_f32 v74, v78, v79
	s_nop 0
	v_cvt_pk_bf16_f32 v75, v80, v81
	v_cvt_pk_bf16_f32 v76, v76, v77
	v_cvt_pk_bf16_f32 v77, v82, v83
	global_store_dwordx4 v[90:91], v[74:77], off
	global_load_dwordx4 v[74:77], v[100:101], off offset:512
	s_nop 0
	global_load_dwordx4 v[78:81], v[100:101], off offset:528
	v_lshl_add_u64 v[82:83], v[156:157], 0, s[46:47]
	v_lshl_add_u64 v[84:85], v[82:83], 2, s[10:11]
	s_waitcnt vmcnt(1)
	v_pk_fma_f32 v[70:71], v[70:71], v[134:135], v[74:75]
	s_waitcnt vmcnt(0)
	v_pk_fma_f32 v[74:75], v[68:69], v[132:133], v[80:81]
	v_pk_fma_f32 v[68:69], v[66:67], v[130:131], v[78:79]
	v_pk_fma_f32 v[72:73], v[72:73], v[136:137], v[76:77]
	v_cvt_pk_bf16_f32 v66, v70, v71
	s_nop 0
	v_cvt_pk_bf16_f32 v67, v72, v73
	v_cvt_pk_bf16_f32 v68, v68, v69
	v_cvt_pk_bf16_f32 v69, v74, v75
	global_store_dwordx4 v[90:91], v[66:69], off offset:256
	global_load_dwordx4 v[66:69], v[84:85], off
	global_load_dwordx4 v[70:73], v[84:85], off offset:16
	v_lshl_add_u64 v[74:75], v[82:83], 1, s[38:39]
	s_waitcnt vmcnt(1)
	v_pk_fma_f32 v[62:63], v[62:63], v[142:143], v[66:67]
	s_waitcnt vmcnt(0)
	v_pk_fma_f32 v[66:67], v[60:61], v[140:141], v[72:73]
	v_pk_fma_f32 v[60:61], v[58:59], v[138:139], v[70:71]
	v_pk_fma_f32 v[64:65], v[64:65], v[144:145], v[68:69]
	v_cvt_pk_bf16_f32 v58, v62, v63
	s_nop 0
	v_cvt_pk_bf16_f32 v59, v64, v65
	v_cvt_pk_bf16_f32 v60, v60, v61
	v_cvt_pk_bf16_f32 v61, v66, v67
	global_store_dwordx4 v[74:75], v[58:61], off
	global_load_dwordx4 v[58:61], v[84:85], off offset:512
	s_nop 0
	global_load_dwordx4 v[62:65], v[84:85], off offset:528
	v_lshl_add_u64 v[66:67], v[156:157], 0, s[48:49]
	v_lshl_add_u64 v[68:69], v[66:67], 2, s[10:11]
	s_waitcnt vmcnt(1)
	v_pk_fma_f32 v[54:55], v[54:55], v[134:135], v[58:59]
	s_waitcnt vmcnt(0)
	v_pk_fma_f32 v[58:59], v[52:53], v[132:133], v[64:65]
	v_pk_fma_f32 v[52:53], v[50:51], v[130:131], v[62:63]
	v_pk_fma_f32 v[56:57], v[56:57], v[136:137], v[60:61]
	v_cvt_pk_bf16_f32 v50, v54, v55
	s_nop 0
	v_cvt_pk_bf16_f32 v51, v56, v57
	v_cvt_pk_bf16_f32 v52, v52, v53
	v_cvt_pk_bf16_f32 v53, v58, v59
	global_store_dwordx4 v[74:75], v[50:53], off offset:256
	global_load_dwordx4 v[50:53], v[68:69], off
	s_nop 0
	global_load_dwordx4 v[54:57], v[68:69], off offset:16
	v_lshl_add_u64 v[58:59], v[66:67], 1, s[38:39]
	s_waitcnt vmcnt(1)
	v_pk_fma_f32 v[46:47], v[46:47], v[142:143], v[50:51]
	s_waitcnt vmcnt(0)
	v_pk_fma_f32 v[50:51], v[44:45], v[140:141], v[56:57]
	v_pk_fma_f32 v[44:45], v[42:43], v[138:139], v[54:55]
	v_pk_fma_f32 v[48:49], v[48:49], v[144:145], v[52:53]
	v_cvt_pk_bf16_f32 v42, v46, v47
	s_nop 0
	v_cvt_pk_bf16_f32 v43, v48, v49
	v_cvt_pk_bf16_f32 v44, v44, v45
	v_cvt_pk_bf16_f32 v45, v50, v51
	global_store_dwordx4 v[58:59], v[42:45], off
	global_load_dwordx4 v[42:45], v[68:69], off offset:512
	s_nop 0
	global_load_dwordx4 v[46:49], v[68:69], off offset:528
	v_lshl_add_u64 v[50:51], v[156:157], 0, s[50:51]
	v_lshl_add_u64 v[52:53], v[50:51], 2, s[10:11]
	s_waitcnt vmcnt(1)
	v_pk_fma_f32 v[38:39], v[38:39], v[134:135], v[42:43]
	s_waitcnt vmcnt(0)
	v_pk_fma_f32 v[42:43], v[36:37], v[132:133], v[48:49]
	v_pk_fma_f32 v[36:37], v[34:35], v[130:131], v[46:47]
	v_pk_fma_f32 v[40:41], v[40:41], v[136:137], v[44:45]
	v_cvt_pk_bf16_f32 v34, v38, v39
	s_nop 0
	v_cvt_pk_bf16_f32 v35, v40, v41
	v_cvt_pk_bf16_f32 v36, v36, v37
	v_cvt_pk_bf16_f32 v37, v42, v43
	global_store_dwordx4 v[58:59], v[34:37], off offset:256
	global_load_dwordx4 v[34:37], v[52:53], off
	global_load_dwordx4 v[38:41], v[52:53], off offset:16
	v_lshl_add_u64 v[42:43], v[50:51], 1, s[38:39]
	s_waitcnt vmcnt(1)
	v_pk_fma_f32 v[30:31], v[30:31], v[142:143], v[34:35]
	s_waitcnt vmcnt(0)
	v_pk_fma_f32 v[34:35], v[28:29], v[140:141], v[40:41]
	v_pk_fma_f32 v[28:29], v[26:27], v[138:139], v[38:39]
	v_pk_fma_f32 v[32:33], v[32:33], v[144:145], v[36:37]
	v_cvt_pk_bf16_f32 v26, v30, v31
	s_nop 0
	v_cvt_pk_bf16_f32 v27, v32, v33
	v_cvt_pk_bf16_f32 v28, v28, v29
	v_cvt_pk_bf16_f32 v29, v34, v35
	global_store_dwordx4 v[42:43], v[26:29], off
	global_load_dwordx4 v[26:29], v[52:53], off offset:512
	s_nop 0
	global_load_dwordx4 v[30:33], v[52:53], off offset:528
	v_lshl_add_u64 v[34:35], v[156:157], 0, s[52:53]
	v_lshl_add_u64 v[36:37], v[34:35], 2, s[10:11]
	s_waitcnt vmcnt(1)
	v_pk_fma_f32 v[22:23], v[22:23], v[134:135], v[26:27]
	s_waitcnt vmcnt(0)
	v_pk_fma_f32 v[26:27], v[20:21], v[132:133], v[32:33]
	v_pk_fma_f32 v[20:21], v[18:19], v[130:131], v[30:31]
	v_pk_fma_f32 v[24:25], v[24:25], v[136:137], v[28:29]
	v_cvt_pk_bf16_f32 v18, v22, v23
	s_nop 0
	v_cvt_pk_bf16_f32 v19, v24, v25
	v_cvt_pk_bf16_f32 v20, v20, v21
	v_cvt_pk_bf16_f32 v21, v26, v27
	global_store_dwordx4 v[42:43], v[18:21], off offset:256
	global_load_dwordx4 v[18:21], v[36:37], off
	s_nop 0
	global_load_dwordx4 v[22:25], v[36:37], off offset:16
	v_lshl_add_u64 v[26:27], v[34:35], 1, s[38:39]
	s_waitcnt vmcnt(1)
	v_pk_fma_f32 v[14:15], v[14:15], v[142:143], v[18:19]
	s_waitcnt vmcnt(0)
	v_pk_fma_f32 v[18:19], v[12:13], v[140:141], v[24:25]
	v_pk_fma_f32 v[12:13], v[10:11], v[138:139], v[22:23]
	v_pk_fma_f32 v[16:17], v[16:17], v[144:145], v[20:21]
	v_cvt_pk_bf16_f32 v10, v14, v15
	s_nop 0
	v_cvt_pk_bf16_f32 v11, v16, v17
	v_cvt_pk_bf16_f32 v12, v12, v13
	v_cvt_pk_bf16_f32 v13, v18, v19
	global_store_dwordx4 v[26:27], v[10:13], off
	global_load_dwordx4 v[10:13], v[36:37], off offset:512
	s_nop 0
	global_load_dwordx4 v[14:17], v[36:37], off offset:528
	s_waitcnt vmcnt(1)
	v_pk_fma_f32 v[6:7], v[6:7], v[134:135], v[10:11]
	s_waitcnt vmcnt(0)
	v_pk_fma_f32 v[10:11], v[4:5], v[132:133], v[16:17]
	v_pk_fma_f32 v[4:5], v[2:3], v[130:131], v[14:15]
	v_pk_fma_f32 v[8:9], v[8:9], v[136:137], v[12:13]
	v_cvt_pk_bf16_f32 v2, v6, v7
	s_nop 0
	v_cvt_pk_bf16_f32 v3, v8, v9
	v_cvt_pk_bf16_f32 v4, v4, v5
	v_cvt_pk_bf16_f32 v5, v10, v11
	global_store_dwordx4 v[26:27], v[2:5], off offset:256
	s_cbranch_vccnz .LBB0_1315
	s_andn2_b64 vcc, exec, s[22:23]
	s_cbranch_vccnz .LBB0_1314
	s_barrier
	s_branch .LBB0_1314
